# gdn_scan chain: LDS fragment reads of batches 2, 4 and 5 issued behind the previous batch's MFMAs (counted lgkmcnt), on top of v85
# speedup vs baseline: 1.0044x; 1.0044x over previous
.LBB0_490:
	s_bitcmp1_b32 s35, 0
	s_cselect_b32 s26, 0xea00, 0
	v_add_u32_e32 v159, s26, v157
	v_add_u32_e32 v190, v159, v155
	ds_read2_b64 v[68:71], v190 offset1:2
	ds_read2_b64 v[84:87], v190 offset0:4 offset1:6
	ds_read2_b64 v[88:91], v190 offset0:8 offset1:10
	ds_read2_b64 v[92:95], v190 offset0:12 offset1:14
	ds_read2_b64 v[96:99], v190 offset0:16 offset1:18
	ds_read2_b64 v[100:103], v190 offset0:20 offset1:22
	ds_read2_b64 v[104:107], v190 offset0:24 offset1:26
	ds_read2_b64 v[108:111], v190 offset0:28 offset1:30
	v_add_u32_e32 v112, 0x2000, v190
	v_add_u32_e32 v182, 0x2000, v190
	v_add_u32_e32 v186, 0x2000, v190
	v_add_u32_e32 v214, 0x2000, v190
	ds_read2_b64 v[112:115], v112 offset0:48 offset1:50
	ds_read2_b64 v[182:185], v182 offset0:52 offset1:54
	ds_read2_b64 v[186:189], v186 offset0:56 offset1:58
	ds_read2_b64 v[214:217], v214 offset0:60 offset1:62
	v_cvt_pk_bf16_f32 v116, v52, v53
	v_cvt_pk_bf16_f32 v117, v54, v55
	v_cvt_pk_bf16_f32 v118, v56, v57
	v_cvt_pk_bf16_f32 v119, v58, v59
	v_cvt_pk_bf16_f32 v120, v60, v61
	v_cvt_pk_bf16_f32 v121, v62, v63
	v_cvt_pk_bf16_f32 v122, v64, v65
	v_cvt_pk_bf16_f32 v123, v66, v67
	v_cvt_pk_bf16_f32 v124, v36, v37
	v_cvt_pk_bf16_f32 v125, v38, v39
	v_cvt_pk_bf16_f32 v126, v40, v41
	v_cvt_pk_bf16_f32 v127, v42, v43
	v_cvt_pk_bf16_f32 v128, v44, v45
	v_cvt_pk_bf16_f32 v129, v46, v47
	v_cvt_pk_bf16_f32 v130, v48, v49
	v_cvt_pk_bf16_f32 v131, v50, v51
	v_cvt_pk_bf16_f32 v132, v20, v21
	v_cvt_pk_bf16_f32 v133, v22, v23
	v_cvt_pk_bf16_f32 v134, v24, v25
	v_cvt_pk_bf16_f32 v135, v26, v27
	v_cvt_pk_bf16_f32 v136, v28, v29
	v_cvt_pk_bf16_f32 v137, v30, v31
	v_cvt_pk_bf16_f32 v138, v32, v33
	v_cvt_pk_bf16_f32 v139, v34, v35
	v_cvt_pk_bf16_f32 v140, v4, v5
	v_cvt_pk_bf16_f32 v141, v6, v7
	v_cvt_pk_bf16_f32 v142, v8, v9
	v_cvt_pk_bf16_f32 v143, v10, v11
	v_cvt_pk_bf16_f32 v144, v12, v13
	v_cvt_pk_bf16_f32 v145, v14, v15
	v_cvt_pk_bf16_f32 v146, v16, v17
	v_cvt_pk_bf16_f32 v147, v18, v19
	s_waitcnt lgkmcnt(4)
	v_mfma_f32_32x32x16_bf16 v[68:83], v[68:71], v[116:119], 0
	v_mfma_f32_32x32x16_bf16 v[68:83], v[84:87], v[120:123], v[68:83]
	v_add_u32_e32 v84, 0x2000, v190
	ds_read2_b64 v[84:87], v84 offset0:32 offset1:34
	v_mfma_f32_32x32x16_bf16 v[68:83], v[88:91], v[124:127], v[68:83]
	v_mfma_f32_32x32x16_bf16 v[68:83], v[92:95], v[128:131], v[68:83]
	v_mfma_f32_32x32x16_bf16 v[68:83], v[96:99], v[132:135], v[68:83]
	v_mfma_f32_32x32x16_bf16 v[68:83], v[100:103], v[136:139], v[68:83]
	v_add_u32_e32 v100, 0x2000, v190
	ds_read2_b64 v[100:103], v100 offset0:36 offset1:38
	v_mfma_f32_32x32x16_bf16 v[68:83], v[104:107], v[140:143], v[68:83]
	v_add_u32_e32 v104, 0x2000, v190
	ds_read2_b64 v[104:107], v104 offset0:40 offset1:42
	v_mfma_f32_32x32x16_bf16 v[68:83], v[108:111], v[144:147], v[68:83]
	v_add_u32_e32 v108, 0x2000, v190
	ds_read2_b64 v[108:111], v108 offset0:44 offset1:46
	v_add_u32_e32 v88, 0x2000, v190
	s_waitcnt lgkmcnt(3)
	v_mfma_f32_32x32x16_bf16 v[84:99], v[84:87], v[116:119], 0
	s_waitcnt lgkmcnt(2)
	v_mfma_f32_32x32x16_bf16 v[84:99], v[100:103], v[120:123], v[84:99]
	s_waitcnt lgkmcnt(1)
	v_mfma_f32_32x32x16_bf16 v[84:99], v[104:107], v[124:127], v[84:99]
	s_waitcnt lgkmcnt(0)
	v_mfma_f32_32x32x16_bf16 v[84:99], v[108:111], v[128:131], v[84:99]
	v_mfma_f32_32x32x16_bf16 v[84:99], v[112:115], v[132:135], v[84:99]
	v_mfma_f32_32x32x16_bf16 v[84:99], v[182:185], v[136:139], v[84:99]
	v_mfma_f32_32x32x16_bf16 v[84:99], v[186:189], v[140:143], v[84:99]
	v_mfma_f32_32x32x16_bf16 v[84:99], v[214:217], v[144:147], v[84:99]
	s_waitcnt vmcnt(32)
	v_mov_b32_e32 v200, v201
	v_sub_f32_e32 v81, v197, v81
	v_sub_f32_e32 v80, v196, v80
	v_sub_f32_e32 v71, v165, v71
	v_sub_f32_e32 v70, v164, v70
	v_sub_f32_e32 v69, v167, v69
	v_sub_f32_e32 v68, v166, v68
	v_cvt_pk_bf16_f32 v106, v80, v81
	s_nop 3
	v_sub_f32_e32 v80, v175, v87
	v_sub_f32_e32 v81, v174, v86
	v_sub_f32_e32 v83, v199, v83
	v_sub_f32_e32 v82, v198, v82
	v_sub_f32_e32 v79, v195, v79
	v_sub_f32_e32 v78, v194, v78
	v_sub_f32_e32 v77, v181, v77
	v_sub_f32_e32 v76, v180, v76
	v_sub_f32_e32 v75, v171, v75
	v_sub_f32_e32 v74, v170, v74
	v_sub_f32_e32 v73, v169, v73
	v_sub_f32_e32 v72, v168, v72
	v_cvt_pk_bf16_f32 v100, v68, v69
	v_cvt_pk_bf16_f32 v101, v70, v71
	v_sub_f32_e32 v68, v179, v91
	v_sub_f32_e32 v69, v178, v90
	v_sub_f32_e32 v70, v177, v89
	v_sub_f32_e32 v71, v176, v88
	v_cvt_pk_bf16_f32 v109, v81, v80
	v_add_u32_e32 v80, 0x4000, v190
	v_cvt_pk_bf16_f32 v102, v72, v73
	v_cvt_pk_bf16_f32 v103, v74, v75
	v_cvt_pk_bf16_f32 v104, v76, v77
	v_cvt_pk_bf16_f32 v105, v78, v79
	v_cvt_pk_bf16_f32 v107, v82, v83
	v_sub_f32_e32 v72, v209, v99
	v_sub_f32_e32 v73, v208, v98
	v_sub_f32_e32 v74, v207, v97
	v_sub_f32_e32 v75, v206, v96
	v_sub_f32_e32 v76, v205, v95
	v_sub_f32_e32 v77, v204, v94
	v_sub_f32_e32 v78, v203, v93
	v_sub_f32_e32 v79, v202, v92
	v_sub_f32_e32 v82, v173, v85
	v_sub_f32_e32 v83, v172, v84
	v_cvt_pk_bf16_f32 v110, v71, v70
	v_cvt_pk_bf16_f32 v111, v69, v68
	ds_read2_b64 v[68:71], v80 offset0:64 offset1:66
	ds_read2_b64 v[84:87], v80 offset0:68 offset1:70
	ds_read2_b64 v[88:91], v80 offset0:72 offset1:74
	ds_read2_b64 v[92:95], v80 offset0:76 offset1:78
	ds_read2_b64 v[96:99], v80 offset0:80 offset1:82
	ds_read2_b64 v[164:167], v80 offset0:84 offset1:86
	ds_read2_b64 v[168:171], v80 offset0:88 offset1:90
	ds_read2_b64 v[172:175], v80 offset0:92 offset1:94
	v_add_u32_e32 v176, 0x6000, v190
	v_add_u32_e32 v180, 0x6000, v190
	v_add_u32_e32 v184, 0x6000, v190
	v_add_u32_e32 v194, 0x6000, v190
	ds_read2_b64 v[176:179], v176 offset0:112 offset1:114
	ds_read2_b64 v[180:183], v180 offset0:116 offset1:118
	ds_read2_b64 v[184:187], v184 offset0:120 offset1:122
	ds_read2_b64 v[194:197], v194 offset0:124 offset1:126
	v_cvt_pk_bf16_f32 v108, v83, v82
	v_cvt_pk_bf16_f32 v112, v79, v78
	v_cvt_pk_bf16_f32 v113, v77, v76
	v_cvt_pk_bf16_f32 v114, v75, v74
	v_cvt_pk_bf16_f32 v115, v73, v72
	s_waitcnt lgkmcnt(11)
	v_mfma_f32_32x32x16_bf16 v[68:83], v[68:71], v[116:119], 0
	s_waitcnt lgkmcnt(10)
	v_mfma_f32_32x32x16_bf16 v[68:83], v[84:87], v[120:123], v[68:83]
	v_add_u32_e32 v84, 0x6000, v190
	ds_read2_b64 v[84:87], v84 offset0:96 offset1:98
	s_waitcnt lgkmcnt(10)
	v_mfma_f32_32x32x16_bf16 v[68:83], v[88:91], v[124:127], v[68:83]
	s_waitcnt lgkmcnt(9)
	v_mfma_f32_32x32x16_bf16 v[68:83], v[92:95], v[128:131], v[68:83]
	s_waitcnt lgkmcnt(8)
	v_mfma_f32_32x32x16_bf16 v[68:83], v[96:99], v[132:135], v[68:83]
	s_waitcnt lgkmcnt(7)
	v_mfma_f32_32x32x16_bf16 v[68:83], v[164:167], v[136:139], v[68:83]
	v_add_u32_e32 v164, 0x6000, v190
	ds_read2_b64 v[164:167], v164 offset0:100 offset1:102
	s_waitcnt lgkmcnt(7)
	v_mfma_f32_32x32x16_bf16 v[68:83], v[168:171], v[140:143], v[68:83]
	v_add_u32_e32 v168, 0x6000, v190
	ds_read2_b64 v[168:171], v168 offset0:104 offset1:106
	s_waitcnt lgkmcnt(7)
	v_mfma_f32_32x32x16_bf16 v[68:83], v[172:175], v[144:147], v[68:83]
	v_add_u32_e32 v172, 0x6000, v190
	ds_read2_b64 v[172:175], v172 offset0:108 offset1:110
	v_add_u32_e32 v88, 0x6000, v190
	s_waitcnt lgkmcnt(3)
	v_mfma_f32_32x32x16_bf16 v[84:99], v[84:87], v[116:119], 0
	v_add_u32_e32 v116, v159, v153
	v_add_u32_e32 v116, 0x8000, v116
	ds_read2_b64 v[116:119], v116 offset0:128 offset1:130
	s_waitcnt lgkmcnt(3)
	v_mfma_f32_32x32x16_bf16 v[84:99], v[164:167], v[120:123], v[84:99]
	v_add_u32_e32 v120, v159, v153
	v_add_u32_e32 v120, 0x8000, v120
	ds_read2_b64 v[120:123], v120 offset0:132 offset1:134
	s_waitcnt lgkmcnt(3)
	v_mfma_f32_32x32x16_bf16 v[84:99], v[168:171], v[124:127], v[84:99]
	v_add_u32_e32 v124, v159, v153
	v_add_u32_e32 v124, 0x8000, v124
	ds_read2_b64 v[124:127], v124 offset0:136 offset1:138
	s_waitcnt lgkmcnt(3)
	v_mfma_f32_32x32x16_bf16 v[84:99], v[172:175], v[128:131], v[84:99]
	v_add_u32_e32 v128, v159, v153
	v_add_u32_e32 v128, 0x8000, v128
	ds_read2_b64 v[128:131], v128 offset0:140 offset1:142
	v_mfma_f32_32x32x16_bf16 v[84:99], v[176:179], v[132:135], v[84:99]
	v_add_u32_e32 v132, v159, v153
	v_add_u32_e32 v132, 0x9000, v132
	ds_read2_b64 v[132:135], v132 offset0:160 offset1:162
	v_mfma_f32_32x32x16_bf16 v[84:99], v[180:183], v[136:139], v[84:99]
	v_add_u32_e32 v136, v159, v153
	v_add_u32_e32 v136, 0x9000, v136
	ds_read2_b64 v[136:139], v136 offset0:164 offset1:166
	v_mfma_f32_32x32x16_bf16 v[84:99], v[184:187], v[140:143], v[84:99]
	v_add_u32_e32 v140, v159, v153
	v_add_u32_e32 v140, 0x9000, v140
	ds_read2_b64 v[140:143], v140 offset0:168 offset1:170
	v_mfma_f32_32x32x16_bf16 v[84:99], v[194:197], v[144:147], v[84:99]
	v_add_u32_e32 v144, v159, v153
	v_add_u32_e32 v144, 0x9000, v144
	ds_read2_b64 v[144:147], v144 offset0:172 offset1:174
	v_add_u32_e32 v159, v159, v153
	s_waitcnt lgkmcnt(7)
	v_mfma_f32_32x32x16_bf16 v[68:83], v[116:119], v[100:103], v[68:83]
	s_waitcnt lgkmcnt(3)
	v_mfma_f32_32x32x16_bf16 v[84:99], v[132:135], v[100:103], v[84:99]
	v_mfma_f32_32x32x16_bf16 v[68:83], v[120:123], v[104:107], v[68:83]
	s_waitcnt lgkmcnt(2)
	v_mfma_f32_32x32x16_bf16 v[84:99], v[136:139], v[104:107], v[84:99]
	v_mfma_f32_32x32x16_bf16 v[68:83], v[124:127], v[108:111], v[68:83]
	s_waitcnt lgkmcnt(1)
	v_mfma_f32_32x32x16_bf16 v[84:99], v[140:143], v[108:111], v[84:99]
	v_mfma_f32_32x32x16_bf16 v[68:83], v[128:131], v[112:115], v[68:83]
	s_waitcnt lgkmcnt(0)
	v_mfma_f32_32x32x16_bf16 v[84:99], v[144:147], v[112:115], v[84:99]
	v_lshl_add_u64 v[116:117], s[6:7], 0, v[162:163]
	s_mov_b32 s26, 0x41a20000
	v_add_co_u32_e32 v218, vcc, s26, v116
	s_nop 1
	v_addc_co_u32_e32 v219, vcc, 0, v117, vcc
	s_mov_b32 s26, 0x41a21000
	v_add_co_u32_e32 v220, vcc, s26, v116
	s_nop 1
	v_addc_co_u32_e32 v221, vcc, 0, v117, vcc
	s_mov_b32 s26, 0x41a24000
	v_add_co_u32_e32 v222, vcc, s26, v116
	s_nop 1
	v_addc_co_u32_e32 v223, vcc, 0, v117, vcc
	s_mov_b32 s26, 0x41a25000
	v_add_co_u32_e32 v224, vcc, s26, v116
	s_nop 1
	v_addc_co_u32_e32 v225, vcc, 0, v117, vcc
	global_load_dword v166, v[218:219], off
	global_load_dword v167, v[218:219], off offset:2048
	global_load_dword v164, v[220:221], off
	global_load_dword v165, v[220:221], off offset:2048
	global_load_dword v168, v[222:223], off
	global_load_dword v169, v[222:223], off offset:2048
	global_load_dword v170, v[224:225], off
	global_load_dword v171, v[224:225], off offset:2048
	s_mov_b32 s26, 0x41a28000
	v_add_co_u32_e32 v218, vcc, s26, v116
	s_nop 1
	v_addc_co_u32_e32 v219, vcc, 0, v117, vcc
	s_mov_b32 s26, 0x41a29000
	v_add_co_u32_e32 v220, vcc, s26, v116
	s_nop 1
	v_addc_co_u32_e32 v221, vcc, 0, v117, vcc
	s_mov_b32 s26, 0x41a2c000
	v_add_co_u32_e32 v222, vcc, s26, v116
	s_nop 1
	v_addc_co_u32_e32 v223, vcc, 0, v117, vcc
	s_mov_b32 s26, 0x41a2d000
	v_add_co_u32_e32 v224, vcc, s26, v116
	s_nop 1
	v_addc_co_u32_e32 v225, vcc, 0, v117, vcc
	global_load_dword v180, v[218:219], off
	global_load_dword v181, v[218:219], off offset:2048
	global_load_dword v194, v[220:221], off
	global_load_dword v195, v[220:221], off offset:2048
	global_load_dword v196, v[222:223], off
	global_load_dword v197, v[222:223], off offset:2048
	global_load_dword v198, v[224:225], off
	global_load_dword v199, v[224:225], off offset:2048
	s_mov_b32 s26, 0x41a30000
	v_add_co_u32_e32 v218, vcc, s26, v116
	s_nop 1
	v_addc_co_u32_e32 v219, vcc, 0, v117, vcc
	s_mov_b32 s26, 0x41a31000
	v_add_co_u32_e32 v220, vcc, s26, v116
	s_nop 1
	v_addc_co_u32_e32 v221, vcc, 0, v117, vcc
	s_mov_b32 s26, 0x41a34000
	v_add_co_u32_e32 v222, vcc, s26, v116
	s_nop 1
	v_addc_co_u32_e32 v223, vcc, 0, v117, vcc
	s_mov_b32 s26, 0x41a35000
	v_add_co_u32_e32 v224, vcc, s26, v116
	s_nop 1
	v_addc_co_u32_e32 v225, vcc, 0, v117, vcc
	global_load_dword v172, v[218:219], off
	global_load_dword v173, v[218:219], off offset:2048
	global_load_dword v174, v[220:221], off
	global_load_dword v175, v[220:221], off offset:2048
	global_load_dword v176, v[222:223], off
	global_load_dword v177, v[222:223], off offset:2048
	global_load_dword v178, v[224:225], off
	global_load_dword v179, v[224:225], off offset:2048
	s_mov_b32 s26, 0x41a38000
	v_add_co_u32_e32 v218, vcc, s26, v116
	s_nop 1
	v_addc_co_u32_e32 v219, vcc, 0, v117, vcc
	s_mov_b32 s26, 0x41a39000
	v_add_co_u32_e32 v220, vcc, s26, v116
	s_nop 1
	v_addc_co_u32_e32 v221, vcc, 0, v117, vcc
	s_mov_b32 s26, 0x41a3c000
	v_add_co_u32_e32 v222, vcc, s26, v116
	s_nop 1
	v_addc_co_u32_e32 v223, vcc, 0, v117, vcc
	s_mov_b32 s26, 0x41a3d000
	v_add_co_u32_e32 v224, vcc, s26, v116
	s_nop 1
	v_addc_co_u32_e32 v225, vcc, 0, v117, vcc
	global_load_dword v202, v[218:219], off
	global_load_dword v203, v[218:219], off offset:2048
	global_load_dword v204, v[220:221], off
	global_load_dword v205, v[220:221], off offset:2048
	global_load_dword v206, v[222:223], off
	global_load_dword v207, v[222:223], off offset:2048
	global_load_dword v208, v[224:225], off
	global_load_dword v209, v[224:225], off offset:2048
	s_add_i32 s35, s35, 1
	s_add_u32 s26, s6, s28
	s_addc_u32 s27, s7, s29
	v_mov_b64_e32 v[232:233], s[26:27]
	global_load_dword v201, v[232:233], off
	s_mov_b32 s26, 0x47200000
	v_add_co_u32_e32 v218, vcc, s26, v116
	s_nop 1
	v_addc_co_u32_e32 v219, vcc, 0, v117, vcc
	s_mov_b32 s26, 0x47201000
	v_add_co_u32_e32 v220, vcc, s26, v116
	s_nop 1
	v_addc_co_u32_e32 v221, vcc, 0, v117, vcc
	s_mov_b32 s26, 0x47204000
	v_add_co_u32_e32 v222, vcc, s26, v116
	s_nop 1
	v_addc_co_u32_e32 v223, vcc, 0, v117, vcc
	s_mov_b32 s26, 0x47205000
	v_add_co_u32_e32 v224, vcc, s26, v116
	s_nop 1
	v_addc_co_u32_e32 v225, vcc, 0, v117, vcc
	global_store_dword v[218:219], v68, off
	global_store_dword v[218:219], v69, off offset:2048
	global_store_dword v[220:221], v70, off
	global_store_dword v[220:221], v71, off offset:2048
	global_store_dword v[222:223], v72, off
	global_store_dword v[222:223], v73, off offset:2048
	global_store_dword v[224:225], v74, off
	global_store_dword v[224:225], v75, off offset:2048
	s_mov_b32 s26, 0x47208000
	v_add_co_u32_e32 v218, vcc, s26, v116
	s_nop 1
	v_addc_co_u32_e32 v219, vcc, 0, v117, vcc
	s_mov_b32 s26, 0x47209000
	v_add_co_u32_e32 v220, vcc, s26, v116
	s_nop 1
	v_addc_co_u32_e32 v221, vcc, 0, v117, vcc
	s_mov_b32 s26, 0x4720c000
	v_add_co_u32_e32 v222, vcc, s26, v116
	s_nop 1
	v_addc_co_u32_e32 v223, vcc, 0, v117, vcc
	s_mov_b32 s26, 0x4720d000
	v_add_co_u32_e32 v224, vcc, s26, v116
	s_nop 1
	v_addc_co_u32_e32 v225, vcc, 0, v117, vcc
	global_store_dword v[218:219], v76, off
	global_store_dword v[218:219], v77, off offset:2048
	global_store_dword v[220:221], v78, off
	global_store_dword v[220:221], v79, off offset:2048
	global_store_dword v[222:223], v80, off
	global_store_dword v[222:223], v81, off offset:2048
	global_store_dword v[224:225], v82, off
	global_store_dword v[224:225], v83, off offset:2048
	s_mov_b32 s26, 0x47210000
	v_add_co_u32_e32 v218, vcc, s26, v116
	s_nop 1
	v_addc_co_u32_e32 v219, vcc, 0, v117, vcc
	s_mov_b32 s26, 0x47211000
	v_add_co_u32_e32 v220, vcc, s26, v116
	s_nop 1
	v_addc_co_u32_e32 v221, vcc, 0, v117, vcc
	s_mov_b32 s26, 0x47214000
	v_add_co_u32_e32 v222, vcc, s26, v116
	s_nop 1
	v_addc_co_u32_e32 v223, vcc, 0, v117, vcc
	s_mov_b32 s26, 0x47215000
	v_add_co_u32_e32 v224, vcc, s26, v116
	s_nop 1
	v_addc_co_u32_e32 v225, vcc, 0, v117, vcc
	global_store_dword v[218:219], v84, off
	global_store_dword v[218:219], v85, off offset:2048
	global_store_dword v[220:221], v86, off
	global_store_dword v[220:221], v87, off offset:2048
	global_store_dword v[222:223], v88, off
	global_store_dword v[222:223], v89, off offset:2048
	global_store_dword v[224:225], v90, off
	global_store_dword v[224:225], v91, off offset:2048
	s_mov_b32 s26, 0x47218000
	v_add_co_u32_e32 v218, vcc, s26, v116
	s_nop 1
	v_addc_co_u32_e32 v219, vcc, 0, v117, vcc
	s_mov_b32 s26, 0x47219000
	v_add_co_u32_e32 v220, vcc, s26, v116
	s_nop 1
	v_addc_co_u32_e32 v221, vcc, 0, v117, vcc
	s_mov_b32 s26, 0x4721c000
	v_add_co_u32_e32 v222, vcc, s26, v116
	s_nop 1
	v_addc_co_u32_e32 v223, vcc, 0, v117, vcc
	s_mov_b32 s26, 0x4721d000
	v_add_co_u32_e32 v224, vcc, s26, v116
	s_nop 1
	v_addc_co_u32_e32 v225, vcc, 0, v117, vcc
	global_store_dword v[218:219], v92, off
	global_store_dword v[218:219], v93, off offset:2048
	global_store_dword v[220:221], v94, off
	global_store_dword v[220:221], v95, off offset:2048
	global_store_dword v[222:223], v96, off
	global_store_dword v[222:223], v97, off offset:2048
	global_store_dword v[224:225], v98, off
	global_store_dword v[224:225], v99, off offset:2048
	v_add_u32_e32 v80, 0xa000, v159
	v_add_u32_e32 v96, 0xb000, v159
	ds_read2_b64 v[68:71], v80 offset0:192 offset1:194
	ds_read2_b64 v[72:75], v80 offset0:196 offset1:198
	ds_read2_b64 v[76:79], v80 offset0:200 offset1:202
	ds_read2_b64 v[80:83], v80 offset0:204 offset1:206
	ds_read2_b64 v[84:87], v96 offset0:224 offset1:226
	ds_read2_b64 v[88:91], v96 offset0:228 offset1:230
	ds_read2_b64 v[92:95], v96 offset0:232 offset1:234
	ds_read2_b64 v[96:99], v96 offset0:236 offset1:238
	v_pk_mul_f32 v[66:67], v[66:67], v[200:201] op_sel_hi:[1,0]
	v_pk_mul_f32 v[64:65], v[64:65], v[200:201] op_sel_hi:[1,0]
	v_pk_mul_f32 v[62:63], v[62:63], v[200:201] op_sel_hi:[1,0]
	v_pk_mul_f32 v[60:61], v[60:61], v[200:201] op_sel_hi:[1,0]
	v_pk_mul_f32 v[58:59], v[58:59], v[200:201] op_sel_hi:[1,0]
	v_pk_mul_f32 v[56:57], v[56:57], v[200:201] op_sel_hi:[1,0]
	v_pk_mul_f32 v[54:55], v[54:55], v[200:201] op_sel_hi:[1,0]
	v_pk_mul_f32 v[52:53], v[52:53], v[200:201] op_sel_hi:[1,0]
	v_pk_mul_f32 v[50:51], v[50:51], v[200:201] op_sel_hi:[1,0]
	v_pk_mul_f32 v[48:49], v[48:49], v[200:201] op_sel_hi:[1,0]
	v_pk_mul_f32 v[46:47], v[46:47], v[200:201] op_sel_hi:[1,0]
	v_pk_mul_f32 v[44:45], v[44:45], v[200:201] op_sel_hi:[1,0]
	v_pk_mul_f32 v[42:43], v[42:43], v[200:201] op_sel_hi:[1,0]
	v_pk_mul_f32 v[40:41], v[40:41], v[200:201] op_sel_hi:[1,0]
	v_pk_mul_f32 v[38:39], v[38:39], v[200:201] op_sel_hi:[1,0]
	v_pk_mul_f32 v[36:37], v[36:37], v[200:201] op_sel_hi:[1,0]
	s_waitcnt lgkmcnt(0)
	v_mfma_f32_32x32x16_bf16 v[52:67], v[68:71], v[100:103], v[52:67]
	v_mfma_f32_32x32x16_bf16 v[36:51], v[84:87], v[100:103], v[36:51]
	v_mfma_f32_32x32x16_bf16 v[52:67], v[72:75], v[104:107], v[52:67]
	v_mfma_f32_32x32x16_bf16 v[36:51], v[88:91], v[104:107], v[36:51]
	v_mfma_f32_32x32x16_bf16 v[52:67], v[76:79], v[108:111], v[52:67]
	v_mfma_f32_32x32x16_bf16 v[36:51], v[92:95], v[108:111], v[36:51]
	v_mfma_f32_32x32x16_bf16 v[52:67], v[80:83], v[112:115], v[52:67]
	v_mfma_f32_32x32x16_bf16 v[36:51], v[96:99], v[112:115], v[36:51]
	v_add_u32_e32 v80, 0xc800, v159
	v_add_u32_e32 v96, 0xd800, v159
	ds_read2_b64 v[68:71], v80 offset1:2
	ds_read2_b64 v[72:75], v80 offset0:4 offset1:6
	ds_read2_b64 v[76:79], v80 offset0:8 offset1:10
	ds_read2_b64 v[80:83], v80 offset0:12 offset1:14
	ds_read2_b64 v[84:87], v96 offset0:32 offset1:34
	ds_read2_b64 v[88:91], v96 offset0:36 offset1:38
	ds_read2_b64 v[92:95], v96 offset0:40 offset1:42
	ds_read2_b64 v[96:99], v96 offset0:44 offset1:46
	v_pk_mul_f32 v[34:35], v[34:35], v[200:201] op_sel_hi:[1,0]
	v_pk_mul_f32 v[32:33], v[32:33], v[200:201] op_sel_hi:[1,0]
	v_pk_mul_f32 v[30:31], v[30:31], v[200:201] op_sel_hi:[1,0]
	v_pk_mul_f32 v[28:29], v[28:29], v[200:201] op_sel_hi:[1,0]
	v_pk_mul_f32 v[26:27], v[26:27], v[200:201] op_sel_hi:[1,0]
	v_pk_mul_f32 v[24:25], v[24:25], v[200:201] op_sel_hi:[1,0]
	v_pk_mul_f32 v[22:23], v[22:23], v[200:201] op_sel_hi:[1,0]
	v_pk_mul_f32 v[20:21], v[20:21], v[200:201] op_sel_hi:[1,0]
	v_pk_mul_f32 v[18:19], v[18:19], v[200:201] op_sel_hi:[1,0]
	v_pk_mul_f32 v[16:17], v[16:17], v[200:201] op_sel_hi:[1,0]
	v_pk_mul_f32 v[14:15], v[14:15], v[200:201] op_sel_hi:[1,0]
	v_pk_mul_f32 v[12:13], v[12:13], v[200:201] op_sel_hi:[1,0]
	v_pk_mul_f32 v[10:11], v[10:11], v[200:201] op_sel_hi:[1,0]
	v_pk_mul_f32 v[8:9], v[8:9], v[200:201] op_sel_hi:[1,0]
	v_pk_mul_f32 v[6:7], v[6:7], v[200:201] op_sel_hi:[1,0]
	v_pk_mul_f32 v[4:5], v[4:5], v[200:201] op_sel_hi:[1,0]
	s_waitcnt lgkmcnt(0)
	v_mfma_f32_32x32x16_bf16 v[20:35], v[68:71], v[100:103], v[20:35]
	v_mfma_f32_32x32x16_bf16 v[4:19], v[84:87], v[100:103], v[4:19]
	v_mfma_f32_32x32x16_bf16 v[20:35], v[72:75], v[104:107], v[20:35]
	v_mfma_f32_32x32x16_bf16 v[4:19], v[88:91], v[104:107], v[4:19]
	v_mfma_f32_32x32x16_bf16 v[20:35], v[76:79], v[108:111], v[20:35]
	v_mfma_f32_32x32x16_bf16 v[4:19], v[92:95], v[108:111], v[4:19]
	v_mfma_f32_32x32x16_bf16 v[20:35], v[80:83], v[112:115], v[20:35]
	v_mfma_f32_32x32x16_bf16 v[4:19], v[96:99], v[112:115], v[4:19]
	s_add_u32 s28, s28, 4
	s_addc_u32 s29, s29, 0
	v_lshl_add_u64 v[162:163], v[162:163], 0, s[38:39]
	s_cmp_eq_u32 s35, 63
	s_barrier
	s_cbranch_scc0 .LBB0_490
	s_waitcnt vmcnt(32)
	v_add_u32_e32 v82, v157, v155
	v_cvt_pk_bf16_f32 v52, v52, v53
	v_cvt_pk_bf16_f32 v53, v54, v55
	v_cvt_pk_bf16_f32 v54, v56, v57
	v_cvt_pk_bf16_f32 v57, v62, v63
	v_cvt_pk_bf16_f32 v62, v8, v9
	v_add_u32_e32 v8, 0xe800, v82
	v_cvt_pk_bf16_f32 v56, v60, v61
	v_cvt_pk_bf16_f32 v36, v36, v37
	v_cvt_pk_bf16_f32 v37, v38, v39
	v_cvt_pk_bf16_f32 v38, v40, v41
	v_cvt_pk_bf16_f32 v39, v42, v43
	v_cvt_pk_bf16_f32 v40, v44, v45
	v_cvt_pk_bf16_f32 v41, v46, v47
	v_cvt_pk_bf16_f32 v42, v48, v49
	v_cvt_pk_bf16_f32 v43, v50, v51
	v_cvt_pk_bf16_f32 v44, v20, v21
	v_cvt_pk_bf16_f32 v45, v22, v23
	v_cvt_pk_bf16_f32 v46, v24, v25
	v_cvt_pk_bf16_f32 v47, v26, v27
	v_cvt_pk_bf16_f32 v48, v28, v29
	v_cvt_pk_bf16_f32 v49, v30, v31
	v_cvt_pk_bf16_f32 v50, v32, v33
	v_cvt_pk_bf16_f32 v51, v34, v35
	v_cvt_pk_bf16_f32 v60, v4, v5
	v_cvt_pk_bf16_f32 v61, v6, v7
	ds_read2_b64 v[4:7], v8 offset0:64 offset1:66
	ds_read2_b64 v[20:23], v8 offset0:68 offset1:70
	ds_read2_b64 v[24:27], v8 offset0:72 offset1:74
	ds_read2_b64 v[28:31], v8 offset0:76 offset1:78
	ds_read2_b64 v[32:35], v8 offset0:80 offset1:82
	ds_read2_b64 v[68:71], v8 offset0:84 offset1:86
	ds_read2_b64 v[72:75], v8 offset0:88 offset1:90
	ds_read2_b64 v[78:81], v8 offset0:92 offset1:94
	s_add_u32 s24, s6, s24
	s_addc_u32 s25, s7, s25
	s_add_u32 s24, s24, s9
	s_addc_u32 s25, s25, 0
	v_lshl_add_u64 v[76:77], v[160:161], 2, s[24:25]
	v_cvt_pk_bf16_f32 v55, v58, v59
	v_cvt_pk_bf16_f32 v58, v64, v65
	v_cvt_pk_bf16_f32 v59, v66, v67
	v_cvt_pk_bf16_f32 v63, v10, v11
	v_cvt_pk_bf16_f32 v64, v12, v13
	v_cvt_pk_bf16_f32 v65, v14, v15
	v_cvt_pk_bf16_f32 v66, v16, v17
	v_cvt_pk_bf16_f32 v67, v18, v19
	s_waitcnt lgkmcnt(7)
	v_mfma_f32_32x32x16_bf16 v[4:19], v[4:7], v[52:55], 0
	s_waitcnt lgkmcnt(6)
	v_mfma_f32_32x32x16_bf16 v[4:19], v[20:23], v[56:59], v[4:19]
	s_waitcnt lgkmcnt(5)
	v_mfma_f32_32x32x16_bf16 v[4:19], v[24:27], v[36:39], v[4:19]
	s_waitcnt lgkmcnt(4)
	v_mfma_f32_32x32x16_bf16 v[4:19], v[28:31], v[40:43], v[4:19]
	s_waitcnt lgkmcnt(3)
	v_mfma_f32_32x32x16_bf16 v[4:19], v[32:35], v[44:47], v[4:19]
	s_waitcnt lgkmcnt(2)
	v_mfma_f32_32x32x16_bf16 v[4:19], v[68:71], v[48:51], v[4:19]
	s_waitcnt lgkmcnt(1)
	v_mfma_f32_32x32x16_bf16 v[4:19], v[72:75], v[60:63], v[4:19]
	s_waitcnt lgkmcnt(0)
	v_mfma_f32_32x32x16_bf16 v[4:19], v[78:81], v[64:67], v[4:19]
	v_add_u32_e32 v20, 0x2100, v82
	v_add_u32_e32 v24, 0xe800, v20
	ds_read2_b64 v[20:23], v24 offset0:64 offset1:66
	ds_read2_b64 v[68:71], v24 offset0:68 offset1:70
	ds_read2_b64 v[72:75], v24 offset0:72 offset1:74
	ds_read2_b64 v[78:81], v24 offset0:76 offset1:78
	ds_read2_b64 v[82:85], v24 offset0:80 offset1:82
	ds_read2_b64 v[86:89], v24 offset0:84 offset1:86
	ds_read2_b64 v[90:93], v24 offset0:88 offset1:90
	ds_read2_b64 v[94:97], v24 offset0:92 offset1:94
	s_waitcnt lgkmcnt(7)
	v_mfma_f32_32x32x16_bf16 v[20:35], v[20:23], v[52:55], 0
	s_waitcnt lgkmcnt(6)
	v_mfma_f32_32x32x16_bf16 v[20:35], v[68:71], v[56:59], v[20:35]
	s_waitcnt lgkmcnt(5)
	v_mfma_f32_32x32x16_bf16 v[20:35], v[72:75], v[36:39], v[20:35]
	s_waitcnt lgkmcnt(4)
	v_mfma_f32_32x32x16_bf16 v[20:35], v[78:81], v[40:43], v[20:35]
	s_waitcnt lgkmcnt(3)
	v_mfma_f32_32x32x16_bf16 v[20:35], v[82:85], v[44:47], v[20:35]
	s_waitcnt lgkmcnt(2)
	v_mfma_f32_32x32x16_bf16 v[20:35], v[86:89], v[48:51], v[20:35]
	s_waitcnt lgkmcnt(1)
	v_mfma_f32_32x32x16_bf16 v[20:35], v[90:93], v[60:63], v[20:35]
	s_waitcnt lgkmcnt(0)
	v_mfma_f32_32x32x16_bf16 v[20:35], v[94:97], v[64:67], v[20:35]
	v_add_f32_e64 v4, v166, -v4
	v_add_f32_e64 v5, v167, -v5
	v_add_f32_e64 v6, v164, -v6
	v_add_f32_e64 v7, v165, -v7
	v_add_f32_e64 v8, v168, -v8
	v_add_f32_e64 v9, v169, -v9
	v_pk_add_f32 v[10:11], v[170:171], v[10:11] neg_lo:[0,1] neg_hi:[0,1]
	v_pk_add_f32 v[12:13], v[180:181], v[12:13] neg_lo:[0,1] neg_hi:[0,1]
	v_pk_add_f32 v[14:15], v[194:195], v[14:15] neg_lo:[0,1] neg_hi:[0,1]
	v_pk_add_f32 v[16:17], v[196:197], v[16:17] neg_lo:[0,1] neg_hi:[0,1]
	v_pk_add_f32 v[18:19], v[198:199], v[18:19] neg_lo:[0,1] neg_hi:[0,1]
	v_cvt_pk_bf16_f32 v68, v4, v5
	v_cvt_pk_bf16_f32 v69, v6, v7
	v_pk_add_f32 v[4:5], v[172:173], v[20:21] neg_lo:[0,1] neg_hi:[0,1]
	v_pk_add_f32 v[6:7], v[174:175], v[22:23] neg_lo:[0,1] neg_hi:[0,1]
	v_add3_u32 v98, s31, v149, v155
	v_cvt_pk_bf16_f32 v70, v8, v9
	v_cvt_pk_bf16_f32 v71, v10, v11
	v_cvt_pk_bf16_f32 v72, v12, v13
	v_cvt_pk_bf16_f32 v73, v14, v15
	v_cvt_pk_bf16_f32 v74, v16, v17
	v_cvt_pk_bf16_f32 v75, v18, v19
	v_pk_add_f32 v[8:9], v[176:177], v[24:25] neg_lo:[0,1] neg_hi:[0,1]
	v_pk_add_f32 v[10:11], v[178:179], v[26:27] neg_lo:[0,1] neg_hi:[0,1]
	v_pk_add_f32 v[12:13], v[202:203], v[28:29] neg_lo:[0,1] neg_hi:[0,1]
	v_pk_add_f32 v[14:15], v[204:205], v[30:31] neg_lo:[0,1] neg_hi:[0,1]
	v_pk_add_f32 v[16:17], v[206:207], v[32:33] neg_lo:[0,1] neg_hi:[0,1]
	v_pk_add_f32 v[18:19], v[208:209], v[34:35] neg_lo:[0,1] neg_hi:[0,1]
	v_cvt_pk_bf16_f32 v78, v4, v5
	v_cvt_pk_bf16_f32 v79, v6, v7
	ds_read2_b64 v[4:7], v98 offset1:2
	ds_read2_b64 v[20:23], v98 offset0:4 offset1:6
	ds_read2_b64 v[24:27], v98 offset0:8 offset1:10
	ds_read2_b64 v[28:31], v98 offset0:12 offset1:14
	ds_read2_b64 v[32:35], v98 offset0:16 offset1:18
	ds_read2_b64 v[82:85], v98 offset0:20 offset1:22
	ds_read2_b64 v[86:89], v98 offset0:24 offset1:26
	ds_read2_b64 v[90:93], v98 offset0:28 offset1:30
	v_cvt_pk_bf16_f32 v80, v8, v9
	v_cvt_pk_bf16_f32 v81, v10, v11
	v_cvt_pk_bf16_f32 v94, v12, v13
	v_cvt_pk_bf16_f32 v95, v14, v15
	v_cvt_pk_bf16_f32 v96, v16, v17
	v_cvt_pk_bf16_f32 v97, v18, v19
	s_waitcnt lgkmcnt(7)
	v_mfma_f32_32x32x16_bf16 v[4:19], v[4:7], v[52:55], 0
	s_waitcnt lgkmcnt(6)
	v_mfma_f32_32x32x16_bf16 v[4:19], v[20:23], v[56:59], v[4:19]
	s_waitcnt lgkmcnt(5)
	v_mfma_f32_32x32x16_bf16 v[4:19], v[24:27], v[36:39], v[4:19]
	s_waitcnt lgkmcnt(4)
	v_mfma_f32_32x32x16_bf16 v[4:19], v[28:31], v[40:43], v[4:19]
	s_waitcnt lgkmcnt(3)
	v_mfma_f32_32x32x16_bf16 v[4:19], v[32:35], v[44:47], v[4:19]
	s_waitcnt lgkmcnt(2)
	v_mfma_f32_32x32x16_bf16 v[4:19], v[82:85], v[48:51], v[4:19]
	s_waitcnt lgkmcnt(1)
	v_mfma_f32_32x32x16_bf16 v[4:19], v[86:89], v[60:63], v[4:19]
	s_waitcnt lgkmcnt(0)
	v_mfma_f32_32x32x16_bf16 v[4:19], v[90:93], v[64:67], v[4:19]
	v_add_u32_e32 v24, 0x2000, v98
	ds_read2_b64 v[20:23], v24 offset0:32 offset1:34
	ds_read2_b64 v[82:85], v24 offset0:36 offset1:38
	ds_read2_b64 v[86:89], v24 offset0:40 offset1:42
	ds_read2_b64 v[90:93], v24 offset0:44 offset1:46
	ds_read2_b64 v[98:101], v24 offset0:48 offset1:50
	ds_read2_b64 v[102:105], v24 offset0:52 offset1:54
	ds_read2_b64 v[106:109], v24 offset0:56 offset1:58
	ds_read2_b64 v[110:113], v24 offset0:60 offset1:62
	s_waitcnt lgkmcnt(7)
	v_mfma_f32_32x32x16_bf16 v[20:35], v[20:23], v[52:55], 0
	s_waitcnt lgkmcnt(6)
	v_mfma_f32_32x32x16_bf16 v[20:35], v[82:85], v[56:59], v[20:35]
	s_waitcnt lgkmcnt(5)
	v_mfma_f32_32x32x16_bf16 v[20:35], v[86:89], v[36:39], v[20:35]
	s_waitcnt lgkmcnt(4)
	v_mfma_f32_32x32x16_bf16 v[20:35], v[90:93], v[40:43], v[20:35]
	s_waitcnt lgkmcnt(3)
	v_mfma_f32_32x32x16_bf16 v[20:35], v[98:101], v[44:47], v[20:35]
	s_waitcnt lgkmcnt(2)
	v_mfma_f32_32x32x16_bf16 v[20:35], v[102:105], v[48:51], v[20:35]
	s_waitcnt lgkmcnt(1)
	v_mfma_f32_32x32x16_bf16 v[20:35], v[106:109], v[60:63], v[20:35]
	s_waitcnt lgkmcnt(0)
	v_mfma_f32_32x32x16_bf16 v[20:35], v[110:113], v[64:67], v[20:35]
	v_add3_u32 v52, s33, v149, v153
	v_add_u32_e32 v64, 0x1000, v52
	ds_read2_b64 v[36:39], v52 offset1:2
	ds_read2_b64 v[40:43], v52 offset0:4 offset1:6
	ds_read2_b64 v[44:47], v52 offset0:8 offset1:10
	ds_read2_b64 v[48:51], v52 offset0:12 offset1:14
	ds_read2_b64 v[52:55], v64 offset0:32 offset1:34
	ds_read2_b64 v[56:59], v64 offset0:36 offset1:38
	ds_read2_b64 v[60:63], v64 offset0:40 offset1:42
	ds_read2_b64 v[64:67], v64 offset0:44 offset1:46
	s_waitcnt lgkmcnt(7)
	v_mfma_f32_32x32x16_bf16 v[4:19], v[36:39], v[68:71], v[4:19]
	s_waitcnt lgkmcnt(3)
	v_mfma_f32_32x32x16_bf16 v[20:35], v[52:55], v[68:71], v[20:35]
	v_mfma_f32_32x32x16_bf16 v[4:19], v[40:43], v[72:75], v[4:19]
	s_waitcnt lgkmcnt(2)
	v_mfma_f32_32x32x16_bf16 v[20:35], v[56:59], v[72:75], v[20:35]
	v_mfma_f32_32x32x16_bf16 v[4:19], v[44:47], v[78:81], v[4:19]
	s_waitcnt lgkmcnt(1)
	v_mfma_f32_32x32x16_bf16 v[20:35], v[60:63], v[78:81], v[20:35]
	v_mfma_f32_32x32x16_bf16 v[4:19], v[48:51], v[94:97], v[4:19]
	s_waitcnt lgkmcnt(0)
	v_mfma_f32_32x32x16_bf16 v[20:35], v[64:67], v[94:97], v[20:35]
	v_lshl_add_u64 v[36:37], v[76:77], 0, v[2:3]
	s_mov_b32 s9, 0x479e0000
	v_add_co_u32_e32 v38, vcc, s9, v36
	s_mov_b32 s9, 0x479e1000
	s_nop 0
	v_addc_co_u32_e32 v39, vcc, 0, v37, vcc
	s_nop 3
	global_store_dword v[38:39], v4, off
	global_store_dword v[38:39], v5, off offset:2048
	v_add_co_u32_e32 v4, vcc, s9, v36
	s_mov_b32 s9, 0x479e4000
	s_nop 0
	v_addc_co_u32_e32 v5, vcc, 0, v37, vcc
	global_store_dword v[4:5], v6, off
	global_store_dword v[4:5], v7, off offset:2048
	v_add_co_u32_e32 v4, vcc, s9, v36
	s_mov_b32 s9, 0x479e5000
	s_nop 0
	v_addc_co_u32_e32 v5, vcc, 0, v37, vcc
	global_store_dword v[4:5], v8, off
	global_store_dword v[4:5], v9, off offset:2048
	v_add_co_u32_e32 v4, vcc, s9, v36
	s_mov_b32 s9, 0x479e8000
	s_nop 0
	v_addc_co_u32_e32 v5, vcc, 0, v37, vcc
	global_store_dword v[4:5], v10, off
	global_store_dword v[4:5], v11, off offset:2048
	v_add_co_u32_e32 v4, vcc, s9, v36
	s_mov_b32 s9, 0x479e9000
	s_nop 0
	v_addc_co_u32_e32 v5, vcc, 0, v37, vcc
	global_store_dword v[4:5], v12, off
	global_store_dword v[4:5], v13, off offset:2048
	v_add_co_u32_e32 v4, vcc, s9, v36
	s_mov_b32 s9, 0x479ec000
	s_nop 0
	v_addc_co_u32_e32 v5, vcc, 0, v37, vcc
	global_store_dword v[4:5], v14, off
	global_store_dword v[4:5], v15, off offset:2048
	v_add_co_u32_e32 v4, vcc, s9, v36
	s_mov_b32 s9, 0x479ed000
	s_nop 0
	v_addc_co_u32_e32 v5, vcc, 0, v37, vcc
	global_store_dword v[4:5], v16, off
	global_store_dword v[4:5], v17, off offset:2048
	v_add_co_u32_e32 v4, vcc, s9, v36
	s_mov_b32 s9, 0x479f0000
	s_nop 0
	v_addc_co_u32_e32 v5, vcc, 0, v37, vcc
	global_store_dword v[4:5], v18, off
	global_store_dword v[4:5], v19, off offset:2048
	v_add_co_u32_e32 v4, vcc, s9, v36
	s_mov_b32 s9, 0x479f1000
	s_nop 0
	v_addc_co_u32_e32 v5, vcc, 0, v37, vcc
	global_store_dword v[4:5], v20, off
	global_store_dword v[4:5], v21, off offset:2048
	v_add_co_u32_e32 v4, vcc, s9, v36
	s_mov_b32 s9, 0x479f4000
	s_nop 0
	v_addc_co_u32_e32 v5, vcc, 0, v37, vcc
	global_store_dword v[4:5], v22, off
	global_store_dword v[4:5], v23, off offset:2048
	v_add_co_u32_e32 v4, vcc, s9, v36
	s_mov_b32 s9, 0x479f5000
	s_nop 0
	v_addc_co_u32_e32 v5, vcc, 0, v37, vcc
	global_store_dword v[4:5], v24, off
	global_store_dword v[4:5], v25, off offset:2048
	v_add_co_u32_e32 v4, vcc, s9, v36
	s_mov_b32 s9, 0x479f8000
	s_nop 0
	v_addc_co_u32_e32 v5, vcc, 0, v37, vcc
	global_store_dword v[4:5], v26, off
	global_store_dword v[4:5], v27, off offset:2048
	v_add_co_u32_e32 v4, vcc, s9, v36
	s_mov_b32 s9, 0x479f9000
	s_nop 0
	v_addc_co_u32_e32 v5, vcc, 0, v37, vcc
	global_store_dword v[4:5], v28, off
	global_store_dword v[4:5], v29, off offset:2048
	v_add_co_u32_e32 v4, vcc, s9, v36
	s_mov_b32 s9, 0x479fc000
	s_nop 0
	v_addc_co_u32_e32 v5, vcc, 0, v37, vcc
	global_store_dword v[4:5], v30, off
	global_store_dword v[4:5], v31, off offset:2048
	v_add_co_u32_e32 v4, vcc, s9, v36
	s_nop 1
	v_addc_co_u32_e32 v5, vcc, 0, v37, vcc
	global_store_dword v[4:5], v32, off
	global_store_dword v[4:5], v33, off offset:2048
	v_add_co_u32_e32 v4, vcc, 0x479fd000, v36
	s_nop 1
	v_addc_co_u32_e32 v5, vcc, 0, v37, vcc
	global_store_dword v[4:5], v34, off
	global_store_dword v[4:5], v35, off offset:2048
	s_mov_b64 s[28:29], 0
	s_waitcnt lgkmcnt(0)
	s_barrier
